# v43 + prep phase: c_kv and k_rope loads of a token issued together with its c_q load (one round trip instead of three)
# baseline (speedup 1.0000x reference)
; __device__ __forceinline__ unsigned f2bf(float f) { unsigned u = __builtin_bit_cast(unsigned, f); return (u + 0x7fffu + ((u >> 16) & 1u)) >> 16; }
; __device__ __forceinline__ void p3_prep(Frame& F) {
;     ...
;         if (lane < 32) {
;             const float x1 = __builtin_bit_cast(float, (unsigned)pr[3840 + lane] << 16), x2 = __builtin_bit_cast(float, (unsigned)pr[3872 + lane] << 16);
;             const float inv = powf(10000.f, -(float)lane / 32.f); const float ang = (float)INI(I_POS)[t] * inv;
;             float sn, cs; sincosf(ang, &sn, &cs);
;             WSP(float, WS_COS)[(size_t)t * 32 + lane] = cs; WSP(float, WS_SIN)[(size_t)t * 32 + lane] = sn;
;             bf16_t* kr = WSP(bf16_t, WS_KR) + (size_t)t * 64;
;             kr[lane] = (bf16_t)f2bf(x1 * cs - x2 * sn); kr[32 + lane] = (bf16_t)f2bf(x2 * cs + x1 * sn);
.LBB0_339:
	s_or_b64 exec, exec, s[8:9]
	s_waitcnt vmcnt(0)
	v_lshlrev_b32_e32 v32, 16, v107
	v_mul_f32_e32 v30, v4, v4
	v_fmamk_f32 v33, v30, 0xb94c1982, v24
	v_fmaak_f32 v33, v30, v33, 0xbe2aaa9d
	v_mul_f32_e32 v33, v30, v33
	v_fmac_f32_e32 v4, v4, v33
	v_fmamk_f32 v33, v30, 0x37d75334, v25
	v_fmaak_f32 v33, v30, v33, 0x3d2aabf7
	v_fmaak_f32 v33, v30, v33, 0xbf000004
	v_fma_f32 v30, v30, v33, 1.0
	v_lshlrev_b32_e32 v33, 30, v31
	v_and_b32_e32 v31, 1, v31
	v_cmp_eq_u32_e32 vcc, 0, v31
	v_xor_b32_e32 v13, v13, v12
	v_and_b32_e32 v34, 0x80000000, v33
	v_cndmask_b32_e32 v31, v30, v4, vcc
	v_xor_b32_e32 v13, v13, v31
	v_xor_b32_e32 v4, 0x80000000, v4
	v_xor_b32_e32 v13, v13, v34
	v_cndmask_b32_e32 v4, v4, v30, vcc
	v_cmp_class_f32_e64 vcc, v12, s57
	v_bitop3_b32 v4, v4, v33, s56 bitop3:0x78
	v_lshlrev_b32_e32 v29, 16, v106
	v_cndmask_b32_e32 v33, v28, v13, vcc
	v_lshl_add_u64 v[12:13], s[22:23], 0, v[6:7]
	v_cndmask_b32_e32 v4, v28, v4, vcc
	v_add_co_u32_e32 v30, vcc, s58, v12
	s_nop 1
	v_addc_co_u32_e32 v31, vcc, 0, v13, vcc
	v_add_co_u32_e32 v12, vcc, 0x600000, v12
	global_store_dword v[30:31], v4, off
	s_nop 0
	v_addc_co_u32_e32 v13, vcc, 0, v13, vcc
	global_store_dword v[12:13], v33, off
	v_mul_f32_e32 v12, v33, v32
	v_fma_f32 v12, v4, v29, -v12
	v_bfe_u32 v13, v12, 16, 1
	v_mul_f32_e32 v29, v33, v29
	v_add3_u32 v30, v12, v13, s59
	v_lshl_add_u64 v[12:13], s[22:23], 0, v[2:3]
	v_fmac_f32_e32 v29, v4, v32
	v_add_co_u32_e32 v12, vcc, 0x800000, v12
	v_bfe_u32 v4, v29, 16, 1
	s_nop 0
	v_addc_co_u32_e32 v13, vcc, 0, v13, vcc
	v_add3_u32 v4, v29, v4, s59
	global_store_short_d16_hi v[12:13], v30, off
	global_store_short_d16_hi v[12:13], v4, off offset:64

; __device__ __forceinline__ void p3_prep(Frame& F) {
;     ...
;         { const u32x4 w = *(const u32x4*)(pr + 3072 + 8 * lane); float s = 0.f;
; #pragma unroll
;           for (int i = 0; i < 4; ++i) { const float a = bf_lo(w[i]), b = bf_hi(w[i]); s += a * a + b * b; }
;           s = wave_sum(s); if (lane == 0) WSP(float, WS_RQ)[t] = 1.f / sqrtf(s * (1.f / 512.f) + EPS_); }
;         { float s = 0.f; if (lane < 32) { const u32x4 w = *(const u32x4*)(pr + 3584 + 8 * lane);
; #pragma unroll
;               for (int i = 0; i < 4; ++i) { const float a = bf_lo(w[i]), b = bf_hi(w[i]); s += a * a + b * b; } }
;           s = wave_sum(s); if (lane == 0) WSP(float, WS_RKV)[t] = 1.f / sqrtf(s * (1.f / 256.f) + EPS_); }
;         if (lane < 32) {
;             const float x1 = __builtin_bit_cast(float, (unsigned)pr[3840 + lane] << 16), x2 = __builtin_bit_cast(float, (unsigned)pr[3872 + lane] << 16);
.LBB0_341:
	s_waitcnt lgkmcnt(0)
	v_lshl_add_u64 v[12:13], s[22:23], 0, v[8:9]
	v_add_co_u32_e32 v30, vcc, 0x1f701000, v12
	s_nop 1
	v_addc_co_u32_e32 v31, vcc, 0, v13, vcc
	global_load_dwordx4 v[100:103], v[30:31], off offset:3072
	global_load_dwordx4 v[30:33], v[30:31], off offset:2048
	v_lshl_add_u64 v[104:105], s[22:23], 0, v[10:11]
	v_add_co_u32_e32 v104, vcc, 0x1f701000, v104
	s_nop 1
	v_addc_co_u32_e32 v105, vcc, 0, v105, vcc
	global_load_ushort v106, v[104:105], off offset:3584
	global_load_ushort v107, v[104:105], off offset:3648
	s_waitcnt vmcnt(2)
	v_lshlrev_b32_e32 v4, 16, v30
	v_and_b32_e32 v29, 0xffff0000, v30
	v_lshlrev_b32_e32 v30, 16, v31
	v_and_b32_e32 v31, 0xffff0000, v31
	v_lshlrev_b32_e32 v34, 16, v32
	v_and_b32_e32 v32, 0xffff0000, v32
	v_mul_f32_e32 v29, v29, v29
	v_mul_f32_e32 v31, v31, v31
	v_lshlrev_b32_e32 v35, 16, v33
	v_and_b32_e32 v33, 0xffff0000, v33
	v_mul_f32_e32 v32, v32, v32
	v_fmac_f32_e32 v29, v4, v4
	v_fmac_f32_e32 v31, v30, v30
	v_mul_f32_e32 v33, v33, v33
	v_fmac_f32_e32 v32, v34, v34
	v_add_f32_e32 v4, v29, v31
	v_add_f32_e32 v4, v32, v4
	v_fmac_f32_e32 v33, v35, v35
	v_add_f32_e32 v4, v33, v4
	s_waitcnt lgkmcnt(0)
	s_nop 1
	v_add_f32_dpp v4, v4, v4 quad_perm:[1,0,3,2] row_mask:0xf bank_mask:0xf bound_ctrl:1
	s_waitcnt lgkmcnt(0)
	s_nop 1
	v_add_f32_dpp v4, v4, v4 quad_perm:[2,3,0,1] row_mask:0xf bank_mask:0xf bound_ctrl:1
	s_waitcnt lgkmcnt(0)
	s_nop 1
	v_add_f32_dpp v4, v4, v4 row_half_mirror row_mask:0xf bank_mask:0xf bound_ctrl:1
	s_waitcnt lgkmcnt(0)
	s_nop 1
	v_add_f32_dpp v4, v4, v4 row_mirror row_mask:0xf bank_mask:0xf bound_ctrl:1
	ds_bpermute_b32 v29, v17, v4
	s_waitcnt lgkmcnt(0)
	v_add_f32_e32 v4, v4, v29
	ds_bpermute_b32 v29, v18, v4
	s_and_saveexec_b64 s[10:11], s[4:5]
	s_cbranch_execz .LBB0_343
	s_waitcnt lgkmcnt(0)
	v_add_f32_e32 v4, v4, v29
	v_fmamk_f32 v4, v4, 0x3b000000, v20
	v_mul_f32_e32 v29, 0x4f800000, v4
	v_cmp_gt_f32_e32 vcc, s19, v4
	s_nop 1
	v_cndmask_b32_e32 v4, v4, v29, vcc
	v_sqrt_f32_e32 v29, v4
	s_nop 0
	v_add_u32_e32 v30, -1, v29
	v_fma_f32 v32, -v30, v29, v4
	v_add_u32_e32 v31, 1, v29
	v_cmp_ge_f32_e64 s[8:9], 0, v32
	s_nop 1
	v_cndmask_b32_e64 v30, v29, v30, s[8:9]
	v_fma_f32 v29, -v31, v29, v4
	v_cmp_lt_f32_e64 s[8:9], 0, v29
	s_nop 1
	v_cndmask_b32_e64 v29, v30, v31, s[8:9]
	v_mul_f32_e32 v30, 0x37800000, v29
	v_cndmask_b32_e32 v29, v29, v30, vcc
	v_cmp_class_f32_e32 vcc, v4, v21
	s_nop 1
	v_cndmask_b32_e32 v4, v29, v4, vcc
	v_div_scale_f32 v29, s[8:9], v4, v4, 1.0
	v_rcp_f32_e32 v30, v29
	s_add_u32 s8, s22, s24
	s_addc_u32 s9, s23, s25
	v_fma_f32 v31, -v29, v30, 1.0
	v_fmac_f32_e32 v30, v31, v30
	v_div_scale_f32 v31, vcc, 1.0, v4, 1.0
	v_mul_f32_e32 v32, v31, v30
	v_fma_f32 v33, -v29, v32, v31
	v_fmac_f32_e32 v32, v33, v30
	v_fma_f32 v29, -v29, v32, v31
	v_div_fmas_f32 v29, v29, v30, v32
	v_div_fixup_f32 v4, v29, v4, 1.0
	global_store_dword v22, v4, s[8:9]
.LBB0_343:
	s_or_b64 exec, exec, s[10:11]
	v_mov_b32_e32 v4, 0
	s_and_saveexec_b64 s[8:9], s[6:7]
	s_cbranch_execz .LBB0_345
	v_mov_b32_e32 v30, v100
	v_mov_b32_e32 v31, v101
	v_mov_b32_e32 v32, v102
	v_mov_b32_e32 v33, v103
	v_lshlrev_b32_e32 v13, 16, v31
	v_lshlrev_b32_e32 v12, 16, v30
	v_and_b32_e32 v31, 0xffff0000, v31
	v_and_b32_e32 v30, 0xffff0000, v30
	v_lshlrev_b32_e32 v35, 16, v33
	v_lshlrev_b32_e32 v34, 16, v32
	v_and_b32_e32 v33, 0xffff0000, v33
	v_and_b32_e32 v32, 0xffff0000, v32
	v_pk_mul_f32 v[30:31], v[30:31], v[30:31]
	v_pk_mul_f32 v[32:33], v[32:33], v[32:33]
	v_pk_fma_f32 v[12:13], v[12:13], v[12:13], v[30:31]
	v_pk_fma_f32 v[30:31], v[34:35], v[34:35], v[32:33]
	v_add_f32_e32 v4, v12, v13
	v_add_f32_e32 v4, v30, v4
	v_add_f32_e32 v4, v31, v4

; __device__ __forceinline__ void p3_prep(Frame& F) {
;     ...
;             const float x1 = __builtin_bit_cast(float, (unsigned)pr[3840 + lane] << 16), x2 = __builtin_bit_cast(float, (unsigned)pr[3872 + lane] << 16);
;             const float inv = powf(10000.f, -(float)lane / 32.f); const float ang = (float)INI(I_POS)[t] * inv;
;             float sn, cs; sincosf(ang, &sn, &cs);
.LBB0_347:
	s_or_b64 exec, exec, s[10:11]
	s_and_saveexec_b64 s[44:45], s[6:7]
	s_cbranch_execz .LBB0_340
	s_load_dwordx2 s[8:9], s[16:17], 0x10
	s_waitcnt lgkmcnt(0)
	v_lshl_add_u64 v[12:13], s[22:23], 0, v[10:11]
	v_add_co_u32_e32 v12, vcc, 0x1f701000, v12
	s_add_u32 s8, s8, s24
	s_addc_u32 s9, s9, s25
	global_load_dword v4, v5, s[8:9]
	v_addc_co_u32_e32 v13, vcc, 0, v13, vcc
	s_waitcnt vmcnt(0)
	v_cvt_f32_i32_e32 v4, v4
	v_mul_f32_e32 v12, v19, v4
	v_and_b32_e32 v13, 0x7fffffff, v12
	v_cmp_nlt_f32_e64 s[8:9], |v12|, s27
	s_and_saveexec_b64 s[10:11], s[8:9]
	s_xor_b64 s[46:47], exec, s[10:11]
	s_cbranch_execz .LBB0_350
	v_lshrrev_b32_e32 v4, 23, v13
	v_add_u32_e32 v4, 0xffffff88, v4
	v_cmp_lt_u32_e32 vcc, 63, v4
	s_nop 1
	v_cndmask_b32_e32 v31, 0, v26, vcc
	v_add_u32_e32 v4, v31, v4
	v_cmp_lt_u32_e64 s[8:9], 31, v4
	s_nop 1
	v_cndmask_b32_e64 v31, 0, v27, s[8:9]
	v_add_u32_e32 v4, v31, v4
	v_cmp_lt_u32_e64 s[10:11], 31, v4
	s_nop 1
	v_cndmask_b32_e64 v31, 0, v27, s[10:11]
	v_add_u32_e32 v31, v31, v4
	v_and_b32_e32 v4, 0x7fffff, v13
	v_or_b32_e32 v44, 0x800000, v4
	v_mad_u64_u32 v[32:33], s[12:13], v44, s36, 0
	v_mov_b32_e32 v4, v33
	v_mad_u64_u32 v[34:35], s[12:13], v44, s37, v[4:5]
	v_mov_b32_e32 v4, v35
	v_mad_u64_u32 v[36:37], s[12:13], v44, s48, v[4:5]
	v_mov_b32_e32 v4, v37
	v_mad_u64_u32 v[38:39], s[12:13], v44, s49, v[4:5]
	v_mov_b32_e32 v4, v39
	v_mad_u64_u32 v[40:41], s[12:13], v44, s50, v[4:5]
	v_mov_b32_e32 v4, v41
	v_mad_u64_u32 v[42:43], s[12:13], v44, s51, v[4:5]
	v_mov_b32_e32 v4, v43
	v_mad_u64_u32 v[44:45], s[12:13], v44, s52, v[4:5]
	v_cndmask_b32_e32 v33, v42, v38, vcc
	v_cndmask_b32_e32 v4, v44, v40, vcc
	v_cndmask_b32_e32 v37, v45, v42, vcc
	v_cndmask_b32_e64 v35, v4, v33, s[8:9]
	v_cndmask_b32_e64 v4, v37, v4, s[8:9]
	v_cndmask_b32_e32 v37, v40, v36, vcc
	v_cndmask_b32_e64 v33, v33, v37, s[8:9]
	v_cndmask_b32_e64 v4, v4, v35, s[10:11]
	v_cndmask_b32_e64 v35, v35, v33, s[10:11]
	v_sub_u32_e32 v39, 32, v31
	v_alignbit_b32 v40, v4, v35, v39
	v_cmp_eq_u32_e64 s[12:13], 0, v31
	v_cndmask_b32_e32 v32, v36, v32, vcc
	s_nop 0
	v_cndmask_b32_e64 v31, v40, v4, s[12:13]
	v_cndmask_b32_e32 v4, v38, v34, vcc
	v_cndmask_b32_e64 v34, v37, v4, s[8:9]
	v_cndmask_b32_e64 v33, v33, v34, s[10:11]
	v_alignbit_b32 v37, v35, v33, v39
	v_cndmask_b32_e64 v35, v37, v35, s[12:13]
	v_bfe_u32 v40, v31, 29, 1
	v_cndmask_b32_e64 v4, v4, v32, s[8:9]
	v_alignbit_b32 v37, v31, v35, 30
	v_sub_u32_e32 v41, 0, v40
	v_cndmask_b32_e64 v4, v34, v4, s[10:11]
	v_xor_b32_e32 v37, v37, v41
	v_alignbit_b32 v32, v33, v4, v39
	v_cndmask_b32_e64 v32, v32, v33, s[12:13]
	v_ffbh_u32_e32 v34, v37
	v_alignbit_b32 v33, v35, v32, 30
	v_min_u32_e32 v34, 32, v34
	v_alignbit_b32 v4, v32, v4, 30
	v_xor_b32_e32 v33, v33, v41
	v_sub_u32_e32 v35, 31, v34
	v_xor_b32_e32 v4, v4, v41
	v_alignbit_b32 v36, v37, v33, v35
	v_alignbit_b32 v4, v33, v4, v35
	v_alignbit_b32 v32, v36, v4, 9
	v_ffbh_u32_e32 v33, v32
	v_min_u32_e32 v33, 32, v33
	v_lshrrev_b32_e32 v38, 29, v31
	v_not_b32_e32 v35, v33
	v_alignbit_b32 v4, v32, v4, v35
	v_lshlrev_b32_e32 v32, 31, v38
	v_or_b32_e32 v35, 0x33000000, v32
	v_add_lshl_u32 v33, v33, v34, 23
	v_lshrrev_b32_e32 v4, 9, v4
	v_sub_u32_e32 v33, v35, v33
	v_or_b32_e32 v32, 0.5, v32
	v_lshlrev_b32_e32 v34, 23, v34
	v_or_b32_e32 v4, v33, v4
	v_lshrrev_b32_e32 v33, 9, v36
	v_sub_u32_e32 v32, v32, v34
	v_or_b32_e32 v32, v33, v32
	v_mul_f32_e32 v33, 0x3fc90fda, v32
	v_fma_f32 v34, v32, s53, -v33
	v_fmac_f32_e32 v34, 0x33a22168, v32
	v_fmac_f32_e32 v34, 0x3fc90fda, v4
	v_lshrrev_b32_e32 v31, 30, v31
	v_add_f32_e32 v4, v33, v34
	v_add_u32_e32 v31, v40, v31
